# g7 without the exact-lgkmcnt rewrite + packed row-sum adds + scale-free conversion fast path (no multiplies, ds_write2) + slice-counter shifts recomputed only on the rare path
# speedup vs baseline: 1.0052x; 1.0052x over previous
; DEVI f32x4 ld_nt(const float* p) { return __builtin_nontemporal_load((const f32x4*)p); }
; DEVI CvSlice cv_slice(const Params& p, int l, int s, int lane) {
;     CvSlice c;
;     if (s < NS_W13) {
;         const int e = s >> 9, r = s & 511, hb = r & 7, mat = (r >> 3) & 1, ks = r >> 4;
;         const float* W = mat ? (e < NE ? p.w3 + ((size_t)l * NE + e) * 1024 * 256 : p.ws3 + (size_t)l * 1024 * 256)
;                              : (e < NE ? p.w1 + ((size_t)l * NE + e) * 1024 * 256 : p.ws1 + (size_t)l * 1024 * 256);
;         const int hc0 = hb * 32;
;         c.src = W + hc0 + (lane & 7) * 4; c.ld = 256; c.dst = p.w13t + (size_t)e * 512 * 1024; c.K = 1024;
;         c.r0 = (hc0 >> 7) * 256 + ((hc0 >> 5) & 3) * 32 + mat * 16; c.k0 = ks * 32; c.perm = 0;
;     } else {
;         s -= NS_W13;
;         const int e = s >> 8, r = s & 255, nb = r & 31, ks = r >> 5;
;         const float* W2 = e < NE ? p.w2 + ((size_t)l * NE + e) * 256 * 1024 : p.ws2 + (size_t)l * 256 * 1024;
;         c.src = W2 + nb * 32 + (lane & 7) * 4; c.ld = 1024; c.dst = p.w2t + (size_t)e * 1024 * 256; c.K = 256; c.r0 = (nb >> 3) * 256 + ((nb & 7) >> 1) * 32 + (nb & 1) * 8; c.k0 = ks * 32; c.perm = 1;
;     }
;     return c;
; }
; DEVI void cv_next(const Params& p, int l, int s, int lane, int stride, CvRun& run) {
;     ...
;     run.c = cv_slice(p, l, s, lane); run.left = 0;
;     if ((stride & 511) == 0) {
;         if (s < NS_W13) { const int e = s >> 9, es = stride >> 9; if (e < NE) { run.left = (NE - 1 - e) / es; run.sstep = (long)es * 1024 * 256; run.dstep = (long)es * 512 * 1024; } }
;         else { const int e = (s - NS_W13) >> 8, es = stride >> 8; if (e < NE) { run.left = (NE - 1 - e) / es; run.sstep = (long)es * 256 * 1024; run.dstep = (long)es * 1024 * 256; } } }
; }
; DEVI void cv_issue(const Params& p, int l, int s, int lane, CvRegs& R, CvRun& run) {
;     R.live = s < NS_SLICES ? 1 : 0;
;     if (R.live) { cv_next(p, l, s, lane, (int)gridDim.x * 8, run); R.c = run.c; const int kq = lane >> 3;
;         const float* sp = R.c.src + (size_t)(R.c.k0 + 2 * kq) * R.c.ld;
;         R.a0 = ld_nt(sp); R.b0 = ld_nt(sp + R.c.ld); R.a1 = ld_nt(sp + (size_t)16 * R.c.ld); R.b1 = ld_nt(sp + (size_t)17 * R.c.ld); }
.LBB0_666:
	s_mul_i32 s98, s89, 0x6000
	s_add_i32 s98, s98, 0
	v_add_u32_e32 v86, s98, v129
	ds_read_b128 v[82:85], v86 offset:12288
	ds_read_b128 v[124:127], v86 offset:18432
	s_cmp_lt_i32 s54, 0x30300
	s_mov_b32 s61, s2
	s_cselect_b64 s[14:15], -1, 0
	s_cmp_gt_i32 s54, 0x302ff
	s_mov_b32 s2, s6
	s_cbranch_scc1 .LBB0_696
	s_cmp_lt_i32 s56, 1
	s_mov_b64 s[16:17], -1
	s_cbranch_scc0 .LBB0_693
	s_lshl_b32 s71, s54, 5
	s_lshl_b32 s84, s54, 4
	s_lshl_b32 s85, s54, 3
	s_lshl_b32 s88, s54, 1
	s_lshl_b32 s70, s54, 10
	s_add_i32 s70, s70, 0xf7f80000
	s_cmp_gt_i32 s54, 0x201ff
	s_cselect_b64 s[16:17], -1, 0
	s_mov_b64 s[6:7], -1
	s_and_b64 vcc, exec, s[16:17]
	s_cbranch_vccz .LBB0_670
	s_add_i32 s6, s54, 0xfffdfe00
	s_lshr_b32 s8, s6, 8
	s_and_b32 s10, s54, 0xe0
	s_cmp_lt_u32 s6, 0x10000
	s_cselect_b64 s[6:7], -1, 0
	s_and_b32 s11, s70, 0x3fc0000
	s_and_b64 s[6:7], s[6:7], exec
	s_cselect_b32 s6, 0xc0, s78
	s_cselect_b32 s11, s11, 0
	s_add_u32 s6, s24, s6
	s_addc_u32 s7, s25, 0
	s_load_dwordx2 s[6:7], s[6:7], 0x0
	s_lshl_b32 s11, s11, 2
	s_load_dwordx2 s[20:21], s[24:25], 0x158
	s_waitcnt lgkmcnt(0)
	s_add_u32 s6, s6, s11
	s_addc_u32 s7, s7, 0
	s_and_b32 s11, s71, 0x3e0
	s_lshl_b32 s11, s11, 2
	s_add_u32 s18, s6, s11
	s_addc_u32 s19, s7, 0
	s_lshl_b64 s[6:7], s[8:9], 19
	s_add_u32 s20, s20, s6
	s_addc_u32 s21, s21, s7
	s_and_b32 s6, s71, 0x300
	s_and_b32 s7, s84, 0x60
	s_or_b32 s6, s6, s7
	s_and_b32 s7, s85, 8
	s_or_b32 s8, s6, s7
	s_mov_b64 s[6:7], 0

; template <bool FIRST> DEVI bool partialSM(f32x16& p0, f32x16& p1, float& m_reg, float& alpha) {
;     float pmax = p0[0];
; #pragma unroll
;     for (int r = 1; r < 16; ++r) pmax = fmaxf(pmax, p0[r]);
; #pragma unroll
;     for (int r = 0; r < 16; ++r) pmax = fmaxf(pmax, p1[r]);
;     { auto rr = __builtin_amdgcn_permlane32_swap(__float_as_uint(pmax), __float_as_uint(pmax), false, false);
;       pmax = fmaxf(__uint_as_float(rr[0]), __uint_as_float(rr[1])); }
;     if (FIRST) { m_reg = pmax; alpha = 1.f;
; #pragma unroll
;         for (int r = 0; r < 16; ++r) { p0[r] = __builtin_amdgcn_exp2f(p0[r] - pmax); p1[r] = p1[r] - pmax; }
;         return false;
;     } else if (__builtin_expect(__all(pmax <= ATT_THR), 1)) { alpha = 1.f;
; #pragma unroll
;         for (int r = 0; r < 16; ++r) p0[r] = __builtin_amdgcn_exp2f(p0[r]);
;         return false;
;     } else { const float d = fmaxf(pmax, 0.f); alpha = __builtin_amdgcn_exp2f(-d); m_reg += d;
; #pragma unroll
;         for (int r = 0; r < 16; ++r) { p0[r] = __builtin_amdgcn_exp2f(p0[r] - d); p1[r] = p1[r] - d; }
;         return true;
;     }
; }
; DEVI void finishSM(f32x16& p0, f32x16& p1, float alpha, float& l_reg, bf16x8& pa0, bf16x8& pa1, bf16x8& pa2, bf16x8& pa3) {
; #pragma unroll
;     for (int r = 0; r < 16; ++r) p1[r] = __builtin_amdgcn_exp2f(p1[r]);
;     f32x2 s2 = (f32x2){p0[0], p0[1]} + (f32x2){p1[0], p1[1]};
; #pragma unroll
;     for (int r = 2; r < 16; r += 2) s2 += (f32x2){p0[r], p0[r + 1]} + (f32x2){p1[r], p1[r + 1]};
;     float ps = s2[0] + s2[1];
;     { auto rr = __builtin_amdgcn_permlane32_swap(__float_as_uint(ps), __float_as_uint(ps), false, false);
;       ps = __uint_as_float(rr[0]) + __uint_as_float(rr[1]); }
;     l_reg = l_reg * alpha + ps;
;     ...
;     PK4(p0, 0, pa0); PK4(p0, 8, pa1); PK4(p1, 0, pa2); PK4(p1, 8, pa3);
;     ...
; }
; DEVI void qkt(f32x16& p0, f32x16& p1, const char* Kb, const bf16x8 (&qr)[6], int r32, int hi, const f32x16& cinit) {
; #pragma unroll
;     for (int d0 = 0; d0 < 6; ++d0) { const int cb = (d0 * 16 + hi * 8) * 2;
;         const bf16x8 k0 = *(const bf16x8*)(Kb + KSWZ(r32, cb)), k1 = *(const bf16x8*)(Kb + KSWZ(32 + r32, cb));
;         p0 = __builtin_amdgcn_mfma_f32_32x32x16_bf16(k0, qr[d0], d0 == 0 ? cinit : p0, 0, 0, 0);
;         p1 = __builtin_amdgcn_mfma_f32_32x32x16_bf16(k1, qr[d0], d0 == 0 ? cinit : p1, 0, 0, 0); }
; }
.LBB0_696:
	v_add_u32_e32 v174, s98, v204
	v_exp_f32_e32 v66, v66
	v_exp_f32_e32 v67, v67
	s_waitcnt lgkmcnt(0)
	v_mfma_f32_32x32x16_bf16 v[98:113], v[82:85], v[150:153], v[34:49]
	v_add_u32_e32 v82, s98, v184
	v_add_u32_e32 v83, s98, v185
	ds_read_b128 v[208:211], v82 offset:12288
	ds_read_b128 v[212:215], v82 offset:18432
	ds_read_b128 v[216:219], v83 offset:12288
	ds_read_b128 v[220:223], v83 offset:18432
	v_exp_f32_e32 v68, v68
	v_exp_f32_e32 v69, v69
	v_exp_f32_e32 v70, v70
	v_exp_f32_e32 v71, v71
	s_waitcnt lgkmcnt(4)
	v_mfma_f32_32x32x16_bf16 v[82:97], v[124:127], v[150:153], v[34:49]
	ds_read_b128 v[124:127], v174 offset:12288
	ds_read_b128 v[224:227], v174 offset:18432
	v_exp_f32_e32 v72, v72
	v_exp_f32_e32 v73, v73
	v_exp_f32_e32 v74, v74
	v_exp_f32_e32 v75, v75
	v_exp_f32_e32 v76, v76
	v_exp_f32_e32 v77, v77
	s_waitcnt lgkmcnt(0)
	v_mfma_f32_32x32x16_bf16 v[98:113], v[208:211], v[138:141], v[98:113]
	v_add_u32_e32 v174, s98, v205
	v_exp_f32_e32 v78, v78
	v_exp_f32_e32 v79, v79
	ds_read_b128 v[228:231], v174 offset:12288
	ds_read_b128 v[232:235], v174 offset:18432
	v_exp_f32_e32 v80, v80
	v_exp_f32_e32 v81, v81
	v_add_u32_e32 v174, s98, v206
	s_waitcnt lgkmcnt(6)
	v_mfma_f32_32x32x16_bf16 v[82:97], v[212:215], v[138:141], v[82:97]
	v_pk_add_f32 v[212:213], v[50:51], v[66:67]
	v_pk_add_f32 v[214:215], v[52:53], v[68:69]
	v_lshl_add_u32 v202, s89, 14, v115
	v_pk_add_f32 v[212:213], v[214:215], v[212:213]
	v_pk_add_f32 v[214:215], v[54:55], v[70:71]
	ds_read_b128 v[208:211], v174 offset:12288
	ds_read_b128 v[236:239], v174 offset:18432
	v_pk_add_f32 v[212:213], v[214:215], v[212:213]
	s_waitcnt lgkmcnt(7)
	v_mfma_f32_32x32x16_bf16 v[98:113], v[216:219], v[134:137], v[98:113]
	v_pk_add_f32 v[214:215], v[56:57], v[72:73]
	v_cvt_pk_bf16_f32 v50, v50, v51
	v_cvt_pk_bf16_f32 v51, v52, v53
	v_cvt_pk_bf16_f32 v52, v54, v55
	v_cvt_pk_bf16_f32 v53, v56, v57
	v_cvt_pk_bf16_f32 v54, v58, v59
	v_pk_add_f32 v[212:213], v[214:215], v[212:213]
	s_waitcnt lgkmcnt(6)
	v_mfma_f32_32x32x16_bf16 v[82:97], v[220:223], v[134:137], v[82:97]
	v_pk_add_f32 v[214:215], v[58:59], v[74:75]
	v_cvt_pk_bf16_f32 v55, v60, v61
	v_cvt_pk_bf16_f32 v56, v62, v63
	v_cvt_pk_bf16_f32 v57, v64, v65
	v_cvt_pk_bf16_f32 v58, v66, v67
	v_cvt_pk_bf16_f32 v59, v68, v69
	v_pk_add_f32 v[212:213], v[214:215], v[212:213]
	s_waitcnt lgkmcnt(5)
	v_mfma_f32_32x32x16_bf16 v[98:113], v[124:127], v[130:133], v[98:113]
	v_pk_add_f32 v[214:215], v[60:61], v[76:77]
	v_pk_add_f32 v[126:127], v[62:63], v[78:79]
	v_pk_add_f32 v[124:125], v[214:215], v[212:213]
	v_cvt_pk_bf16_f32 v60, v70, v71
	v_cvt_pk_bf16_f32 v61, v72, v73
	v_cvt_pk_bf16_f32 v62, v74, v75
	v_cvt_pk_bf16_f32 v63, v76, v77
	s_waitcnt lgkmcnt(4)
	v_mfma_f32_32x32x16_bf16 v[82:97], v[224:227], v[130:133], v[82:97]
	v_pk_add_f32 v[124:125], v[126:127], v[124:125]
	v_pk_add_f32 v[126:127], v[64:65], v[80:81]
	v_cvt_pk_bf16_f32 v64, v78, v79
	v_cvt_pk_bf16_f32 v65, v80, v81
	ds_read_b64_tr_b16 v[66:67], v202 offset:0
	ds_read_b64_tr_b16 v[68:69], v202 offset:0x400
	ds_read_b64_tr_b16 v[70:71], v202 offset:0x800
	s_waitcnt lgkmcnt(0)
	v_mfma_f32_32x32x16_bf16 v[98:113], v[228:231], v[146:149], v[98:113]
	ds_read_b64_tr_b16 v[72:73], v202 offset:0xc00
	ds_read_b64_tr_b16 v[74:75], v202 offset:0x1000
	ds_read_b64_tr_b16 v[76:77], v202 offset:0x1400
	ds_read_b64_tr_b16 v[78:79], v202 offset:0x1800
	ds_read_b64_tr_b16 v[80:81], v202 offset:0x1c00
	v_pk_add_f32 v[124:125], v[126:127], v[124:125]
	s_waitcnt lgkmcnt(2)
	v_mfma_f32_32x32x16_bf16 v[82:97], v[232:235], v[146:149], v[82:97]
	v_pk_add_f32 v[124:125], v[124:125], v[124:125] op_sel:[0,1] op_sel_hi:[1,0]
	s_nop 0
	v_mov_b32_e32 v125, v124
	s_nop 1
	v_permlane32_swap_b32_e32 v124, v125
	s_waitcnt lgkmcnt(1)
	v_mfma_f32_32x32x16_bf16 v[98:113], v[208:211], v[142:145], v[98:113]
	ds_read_b64_tr_b16 v[208:209], v202 offset:0x200
	ds_read_b64_tr_b16 v[210:211], v202 offset:0x600
	ds_read_b64_tr_b16 v[212:213], v202 offset:0xa00
	ds_read_b64_tr_b16 v[214:215], v202 offset:0xe00
	ds_read_b64_tr_b16 v[216:217], v202 offset:0x1200
	ds_read_b64_tr_b16 v[218:219], v202 offset:0x1600
	ds_read_b64_tr_b16 v[220:221], v202 offset:0x1a00
	s_waitcnt lgkmcnt(0)
	v_mfma_f32_32x32x16_bf16 v[82:97], v[236:239], v[142:145], v[82:97]
	ds_read_b64_tr_b16 v[222:223], v202 offset:0x1e00
	s_waitcnt lgkmcnt(8)
	v_mfma_f32_32x32x16_bf16 v[18:33], v[50:53], v[66:69], v[18:33]
	s_waitcnt lgkmcnt(0)
	v_mfma_f32_32x32x16_bf16 v[18:33], v[54:57], v[70:73], v[18:33]
	v_mfma_f32_32x32x16_bf16 v[18:33], v[58:61], v[74:77], v[18:33]
	v_mfma_f32_32x32x16_bf16 v[18:33], v[62:65], v[78:81], v[18:33]
	v_mfma_f32_32x32x16_bf16 v[2:17], v[50:53], v[208:211], v[2:17]
	s_nop 4
	v_max_f32_e32 v249, v99, v99
	v_max_f32_e32 v250, v98, v98
	v_max_f32_e32 v249, v250, v249
	v_max3_f32 v249, v249, v100, v101
	v_max3_f32 v249, v249, v102, v103
	v_max3_f32 v251, v249, v104, v105
	v_max3_f32 v251, v251, v106, v107
	v_exp_f32_e32 v50, v98
	v_exp_f32_e32 v51, v99
	v_exp_f32_e32 v52, v100
	v_exp_f32_e32 v53, v101
	v_mov_b64_e32 v[66:67], v[82:83]
	v_mov_b64_e32 v[68:69], v[84:85]
	v_mfma_f32_32x32x16_bf16 v[2:17], v[54:57], v[212:215], v[2:17]
	v_max3_f32 v251, v251, v108, v109
	v_max3_f32 v251, v251, v110, v111
	v_max3_f32 v251, v251, v112, v113
	v_max3_f32 v251, v251, v82, v83
	v_max3_f32 v251, v251, v84, v85
	v_max3_f32 v251, v251, v86, v87
	v_max3_f32 v251, v251, v88, v89
	v_exp_f32_e32 v54, v102
	v_exp_f32_e32 v55, v103
	v_exp_f32_e32 v56, v104
	v_exp_f32_e32 v57, v105
	v_mov_b64_e32 v[70:71], v[86:87]
	v_mov_b64_e32 v[72:73], v[88:89]
	v_mfma_f32_32x32x16_bf16 v[2:17], v[58:61], v[216:219], v[2:17]
	v_max3_f32 v251, v251, v90, v91
	v_max3_f32 v251, v251, v92, v93
	v_max3_f32 v251, v251, v94, v95
	v_max3_f32 v251, v251, v96, v97
	v_mov_b32_e32 v252, v251
	s_nop 1
	v_permlane32_swap_b32_e32 v251, v252
	v_exp_f32_e32 v58, v106
	v_exp_f32_e32 v59, v107
	v_exp_f32_e32 v60, v108
	v_exp_f32_e32 v61, v109
	v_mov_b64_e32 v[74:75], v[90:91]
	v_mov_b64_e32 v[76:77], v[92:93]
	v_mfma_f32_32x32x16_bf16 v[2:17], v[62:65], v[220:223], v[2:17]
	v_exp_f32_e32 v62, v110
	v_exp_f32_e32 v63, v111
	v_exp_f32_e32 v64, v112
	v_exp_f32_e32 v65, v113
	v_mov_b64_e32 v[78:79], v[94:95]
	v_mov_b64_e32 v[80:81], v[96:97]
	v_max_f32_e32 v252, v252, v252
	v_max_f32_e32 v251, v251, v251
	v_max_f32_e32 v126, v251, v252
	v_cmp_ge_f32_e32 vcc, s79, v126
	s_cmp_lg_u64 vcc, exec
	s_cselect_b64 s[6:7], -1, 0
	s_cbranch_scc1 .LBB0_705
	v_mov_b32_e32 v208, 1.0
	v_mov_b32_e32 v209, v203
	s_branch .LBB0_699

; template <bool FIRST> DEVI bool partialSM(f32x16& p0, f32x16& p1, float& m_reg, float& alpha) {
;     float pmax = p0[0];
; #pragma unroll
;     for (int r = 1; r < 16; ++r) pmax = fmaxf(pmax, p0[r]);
; #pragma unroll
;     for (int r = 0; r < 16; ++r) pmax = fmaxf(pmax, p1[r]);
;     { auto rr = __builtin_amdgcn_permlane32_swap(__float_as_uint(pmax), __float_as_uint(pmax), false, false);
;       pmax = fmaxf(__uint_as_float(rr[0]), __uint_as_float(rr[1])); }
;     if (FIRST) { m_reg = pmax; alpha = 1.f;
; #pragma unroll
;         for (int r = 0; r < 16; ++r) { p0[r] = __builtin_amdgcn_exp2f(p0[r] - pmax); p1[r] = p1[r] - pmax; }
;         return false;
;     } else if (__builtin_expect(__all(pmax <= ATT_THR), 1)) { alpha = 1.f;
; #pragma unroll
;         for (int r = 0; r < 16; ++r) p0[r] = __builtin_amdgcn_exp2f(p0[r]);
;         return false;
;     } else { const float d = fmaxf(pmax, 0.f); alpha = __builtin_amdgcn_exp2f(-d); m_reg += d;
; #pragma unroll
;         for (int r = 0; r < 16; ++r) { p0[r] = __builtin_amdgcn_exp2f(p0[r] - d); p1[r] = p1[r] - d; }
;         return true;
;     }
; }
; DEVI void finishSM(f32x16& p0, f32x16& p1, float alpha, float& l_reg, bf16x8& pa0, bf16x8& pa1, bf16x8& pa2, bf16x8& pa3) {
; #pragma unroll
;     for (int r = 0; r < 16; ++r) p1[r] = __builtin_amdgcn_exp2f(p1[r]);
;     f32x2 s2 = (f32x2){p0[0], p0[1]} + (f32x2){p1[0], p1[1]};
; #pragma unroll
;     for (int r = 2; r < 16; r += 2) s2 += (f32x2){p0[r], p0[r + 1]} + (f32x2){p1[r], p1[r + 1]};
;     float ps = s2[0] + s2[1];
;     { auto rr = __builtin_amdgcn_permlane32_swap(__float_as_uint(ps), __float_as_uint(ps), false, false);
;       ps = __uint_as_float(rr[0]) + __uint_as_float(rr[1]); }
;     l_reg = l_reg * alpha + ps;
;     ...
;     PK4(p0, 0, pa0); PK4(p0, 8, pa1); PK4(p1, 0, pa2); PK4(p1, 8, pa3);
;     ...
; }
; DEVI void qkt(f32x16& p0, f32x16& p1, const char* Kb, const bf16x8 (&qr)[6], int r32, int hi, const f32x16& cinit) {
; #pragma unroll
;     for (int d0 = 0; d0 < 6; ++d0) { const int cb = (d0 * 16 + hi * 8) * 2;
;         const bf16x8 k0 = *(const bf16x8*)(Kb + KSWZ(r32, cb)), k1 = *(const bf16x8*)(Kb + KSWZ(32 + r32, cb));
;         p0 = __builtin_amdgcn_mfma_f32_32x32x16_bf16(k0, qr[d0], d0 == 0 ? cinit : p0, 0, 0, 0);
;         p1 = __builtin_amdgcn_mfma_f32_32x32x16_bf16(k1, qr[d0], d0 == 0 ? cinit : p1, 0, 0, 0); }
; }
.LBB0_702:
	s_mul_i32 s98, s2, 0x6000
	s_add_i32 s98, s96, s98
	s_lshl_b32 s99, s2, 14
	s_add_i32 s99, s97, s99
	s_mul_i32 s6, s61, 0x6000
	s_add_i32 s6, s6, 0
	v_add_u32_e32 v86, s6, v129
	v_lshl_add_u64 v[250:251], v[118:119], 0, s[12:13]
	s_mov_b32 m0, s98
	s_barrier
	ds_read_b128 v[82:85], v86
	ds_read_b128 v[210:213], v86 offset:6144
	global_load_lds_dwordx4 v[250:251], off
	v_exp_f32_e32 v66, v66
	s_waitcnt lgkmcnt(0)
	v_mfma_f32_32x32x16_bf16 v[98:113], v[82:85], v[150:153], v[34:49]
	v_add_u32_e32 v126, s6, v184
	v_lshl_add_u64 v[250:251], v[120:121], 0, s[12:13]
	s_add_i32 m0, s98, 0x2000
	v_exp_f32_e32 v67, v67
	v_exp_f32_e32 v68, v68
	global_load_lds_dwordx4 v[250:251], off
	v_exp_f32_e32 v69, v69
	v_exp_f32_e32 v70, v70
	v_exp_f32_e32 v71, v71
	v_exp_f32_e32 v72, v72
	v_mfma_f32_32x32x16_bf16 v[82:97], v[210:213], v[150:153], v[34:49]
	ds_read_b128 v[210:213], v126
	ds_read_b128 v[214:217], v126 offset:6144
	v_add_u32_e32 v126, s6, v185
	v_lshl_add_u64 v[250:251], v[122:123], 0, s[12:13]
	s_add_i32 m0, s98, 0x4000
	v_exp_f32_e32 v73, v73
	v_exp_f32_e32 v74, v74
	global_load_lds_dwordx4 v[250:251], off
	v_exp_f32_e32 v75, v75
	v_exp_f32_e32 v76, v76
	v_exp_f32_e32 v77, v77
	s_waitcnt lgkmcnt(0)
	v_mfma_f32_32x32x16_bf16 v[98:113], v[210:213], v[138:141], v[98:113]
	s_mov_b32 m0, s99
	v_exp_f32_e32 v78, v78
	v_exp_f32_e32 v79, v79
	v_lshl_add_u64 v[250:251], v[116:117], 0, s[40:41]
	global_load_lds_dwordx4 v[116:117], off
	s_add_i32 m0, s99, 0x2000
	v_exp_f32_e32 v80, v80
	v_exp_f32_e32 v81, v81
	v_add_u32_e32 v174, 0x2000, v202
	global_load_lds_dwordx4 v[250:251], off
	v_mfma_f32_32x32x16_bf16 v[82:97], v[214:217], v[138:141], v[82:97]
	ds_read_b128 v[210:213], v126
	ds_read_b128 v[214:217], v126 offset:6144
	v_add_u32_e32 v126, s6, v204
	s_waitcnt lgkmcnt(0)
	v_mfma_f32_32x32x16_bf16 v[98:113], v[210:213], v[134:137], v[98:113]
	ds_read_b128 v[210:213], v126
	ds_read_b128 v[218:221], v126 offset:6144
	v_add_u32_e32 v126, s6, v205
	v_mfma_f32_32x32x16_bf16 v[82:97], v[214:217], v[134:137], v[82:97]
	ds_read_b128 v[214:217], v126
	ds_read_b128 v[222:225], v126 offset:6144
	v_add_u32_e32 v126, s6, v206
	ds_read_b128 v[226:229], v126
	ds_read_b128 v[230:233], v126 offset:6144
	v_pk_add_f32 v[126:127], v[50:51], v[66:67]
	v_cvt_pk_bf16_f32 v50, v50, v51
	v_cvt_pk_bf16_f32 v51, v52, v53
	s_waitcnt lgkmcnt(0)
	v_mfma_f32_32x32x16_bf16 v[98:113], v[210:213], v[130:133], v[98:113]
	v_pk_add_f32 v[210:211], v[52:53], v[68:69]
	v_cvt_pk_bf16_f32 v52, v54, v55
	v_cvt_pk_bf16_f32 v53, v56, v57
	v_pk_add_f32 v[126:127], v[210:211], v[126:127]
	v_pk_add_f32 v[210:211], v[54:55], v[70:71]
	v_cvt_pk_bf16_f32 v54, v58, v59
	v_mfma_f32_32x32x16_bf16 v[82:97], v[218:221], v[130:133], v[82:97]
	v_pk_add_f32 v[126:127], v[210:211], v[126:127]
	v_pk_add_f32 v[210:211], v[56:57], v[72:73]
	v_cvt_pk_bf16_f32 v55, v60, v61
	v_cvt_pk_bf16_f32 v56, v62, v63
	v_cvt_pk_bf16_f32 v57, v64, v65
	v_pk_add_f32 v[126:127], v[210:211], v[126:127]
	v_pk_add_f32 v[210:211], v[58:59], v[74:75]
	v_cvt_pk_bf16_f32 v58, v66, v67
	v_cvt_pk_bf16_f32 v59, v68, v69
	v_mfma_f32_32x32x16_bf16 v[98:113], v[214:217], v[146:149], v[98:113]
	v_pk_add_f32 v[126:127], v[210:211], v[126:127]
	v_pk_add_f32 v[210:211], v[60:61], v[76:77]
	v_cvt_pk_bf16_f32 v60, v70, v71
	v_cvt_pk_bf16_f32 v61, v72, v73
	v_pk_add_f32 v[126:127], v[210:211], v[126:127]
	v_pk_add_f32 v[210:211], v[62:63], v[78:79]
	v_cvt_pk_bf16_f32 v62, v74, v75
	v_cvt_pk_bf16_f32 v63, v76, v77
	v_mfma_f32_32x32x16_bf16 v[82:97], v[222:225], v[146:149], v[82:97]
	v_pk_add_f32 v[126:127], v[210:211], v[126:127]
	v_pk_add_f32 v[210:211], v[64:65], v[80:81]
	v_cvt_pk_bf16_f32 v64, v78, v79
	v_cvt_pk_bf16_f32 v65, v80, v81
	ds_read_b64_tr_b16 v[66:67], v174 offset:0
	ds_read_b64_tr_b16 v[68:69], v174 offset:0x400
	ds_read_b64_tr_b16 v[70:71], v174 offset:0x800
	ds_read_b64_tr_b16 v[72:73], v174 offset:0xc00
	ds_read_b64_tr_b16 v[74:75], v174 offset:0x1000
	ds_read_b64_tr_b16 v[76:77], v174 offset:0x1400
	ds_read_b64_tr_b16 v[78:79], v174 offset:0x1800
	ds_read_b64_tr_b16 v[80:81], v174 offset:0x1c00
	v_pk_add_f32 v[126:127], v[210:211], v[126:127]
	ds_read_b64_tr_b16 v[210:211], v174 offset:0x200
	ds_read_b64_tr_b16 v[212:213], v174 offset:0x600
	ds_read_b64_tr_b16 v[214:215], v174 offset:0xa00
	v_mfma_f32_32x32x16_bf16 v[98:113], v[226:229], v[142:145], v[98:113]
	ds_read_b64_tr_b16 v[216:217], v174 offset:0xe00
	ds_read_b64_tr_b16 v[218:219], v174 offset:0x1200
	ds_read_b64_tr_b16 v[220:221], v174 offset:0x1600
	ds_read_b64_tr_b16 v[222:223], v174 offset:0x1a00
	ds_read_b64_tr_b16 v[224:225], v174 offset:0x1e00
	v_pk_add_f32 v[126:127], v[126:127], v[126:127] op_sel:[0,1] op_sel_hi:[1,0]
	s_waitcnt lgkmcnt(8)
	v_mfma_f32_32x32x16_bf16 v[82:97], v[230:233], v[142:145], v[82:97]
	v_mov_b32_e32 v127, v126
	s_nop 1
	v_permlane32_swap_b32_e32 v126, v127
	v_mfma_f32_32x32x16_bf16 v[18:33], v[50:53], v[66:69], v[18:33]
	s_waitcnt lgkmcnt(0)
	v_mfma_f32_32x32x16_bf16 v[18:33], v[54:57], v[70:73], v[18:33]
	v_mfma_f32_32x32x16_bf16 v[18:33], v[58:61], v[74:77], v[18:33]
	v_mfma_f32_32x32x16_bf16 v[18:33], v[62:65], v[78:81], v[18:33]
	v_mfma_f32_32x32x16_bf16 v[2:17], v[50:53], v[210:213], v[2:17]
	s_nop 0
	v_max_f32_e32 v249, v99, v99
	v_max_f32_e32 v250, v98, v98
	v_max_f32_e32 v249, v250, v249
	v_max3_f32 v249, v249, v100, v101
	v_max3_f32 v249, v249, v102, v103
	v_max3_f32 v251, v249, v104, v105
	v_max3_f32 v251, v251, v106, v107
	v_exp_f32_e32 v50, v98
	v_exp_f32_e32 v51, v99
	v_exp_f32_e32 v52, v100
	v_exp_f32_e32 v53, v101
	v_mov_b64_e32 v[66:67], v[82:83]
	v_mov_b64_e32 v[68:69], v[84:85]
	v_mfma_f32_32x32x16_bf16 v[2:17], v[54:57], v[214:217], v[2:17]
	v_max3_f32 v251, v251, v108, v109
	v_max3_f32 v251, v251, v110, v111
	v_max3_f32 v251, v251, v112, v113
	v_max3_f32 v251, v251, v82, v83
	v_max3_f32 v251, v251, v84, v85
	v_max3_f32 v251, v251, v86, v87
	v_max3_f32 v251, v251, v88, v89
	v_exp_f32_e32 v54, v102
	v_exp_f32_e32 v55, v103
	v_exp_f32_e32 v56, v104
	v_exp_f32_e32 v57, v105
	v_mov_b64_e32 v[70:71], v[86:87]
	v_mov_b64_e32 v[72:73], v[88:89]
	v_mfma_f32_32x32x16_bf16 v[2:17], v[58:61], v[218:221], v[2:17]
	v_max3_f32 v251, v251, v90, v91
	v_max3_f32 v251, v251, v92, v93
	v_max3_f32 v251, v251, v94, v95
	v_max3_f32 v251, v251, v96, v97
	v_mov_b32_e32 v252, v251
	s_nop 1
	v_permlane32_swap_b32_e32 v251, v252
	v_exp_f32_e32 v58, v106
	v_exp_f32_e32 v59, v107
	v_exp_f32_e32 v60, v108
	v_exp_f32_e32 v61, v109
	v_mov_b64_e32 v[74:75], v[90:91]
	v_mov_b64_e32 v[76:77], v[92:93]
	v_mfma_f32_32x32x16_bf16 v[2:17], v[62:65], v[222:225], v[2:17]
	v_exp_f32_e32 v62, v110
	v_exp_f32_e32 v63, v111
	v_exp_f32_e32 v64, v112
	v_exp_f32_e32 v65, v113
	v_mov_b64_e32 v[78:79], v[94:95]
	v_mov_b64_e32 v[80:81], v[96:97]
	v_max_f32_e32 v252, v252, v252
	v_max_f32_e32 v251, v251, v251
	v_max_f32_e32 v174, v251, v252
	v_cmp_ge_f32_e32 vcc, s79, v174
	s_cmp_lg_u64 vcc, exec
	s_cselect_b64 s[6:7], -1, 0
	s_cbranch_scc1 .LBB0_711
	v_mov_b32_e32 v202, 1.0
	v_mov_b32_e32 v203, v209
	s_branch .LBB0_716

; #define VM0() asm volatile("s_waitcnt vmcnt(0)" ::: "memory")
; #define B_RESC(a, rare) do { if (rare) { if (hi == 0) al_l[r32] = (a); asm volatile("s_waitcnt lgkmcnt(0)" ::: "memory"); __builtin_amdgcn_wave_barrier(); \
;         _Pragma("unroll") for (int _d = 0; _d < 2; ++_d) _Pragma("unroll") for (int _r = 0; _r < 16; ++_r) o[_d][_r] *= al_l[crow(_r, hi)]; C_SPLAT(); } } while (0)
; DEVI void attn_unit8(const Params& p, char* smem, int unit, int l, int& cvs  , CvRun& crun) {
;     ...
;     for (int T = 0; T + 1 < NTILE; ++T) {
;         const char* Kb = K_lds + s0 * 24576; const int vb = vb0 + s0 * 16384;
;         CvRegs cvr; cv_issue(p, l, cvs, lane, cvr, crun); cvs += (int)gridDim.x * 8;
;         qkt(pB0, pB1, Kb + 12288, qr, r32, hi, cinit);
;         finishSM(pA0, pA1, alA, l_reg, pa0, pa1, pa2, pa3);
;         pv_both(o[0], o[1], vb, pa0, pa1, pa2, pa3);
;         { const bool rr_ = partialSM<false>(pB0, pB1, m_reg, alB); B_RESC(alB, rr_); }
;         cv_finish(smem + 124928 + wid * 2304, lane, cvr);
;         if (cvr.live) asm volatile("s_waitcnt vmcnt(2)" ::: "memory"); else VM0();
;         __syncthreads();
;         if (T + 2 < NTILE) B_DMA(T + 2, s2);
;         qkt(pA0, pA1, K_lds + s1 * 24576, qr, r32, hi, cinit);
;         finishSM(pB0, pB1, alB, l_reg, pa0, pa1, pa2, pa3);
;         pv_both(o[0], o[1], vb + 8192, pa0, pa1, pa2, pa3);
;         { const bool rr_ = partialSM<false>(pA0, pA1, m_reg, alA); B_RESC(alA, rr_); }
;         { const int t = s0; s0 = s1; s1 = s2; s2 = t; }
;     }
.LBB0_716:
	s_add_i32 s54, s54, s86
	v_add_f32_e32 v82, v124, v125
	s_add_u32 s12, s12, 0x6000
	v_fmac_f32_e32 v82, v188, v207
	v_add_f32_e32 v188, v126, v127
	s_addc_u32 s13, s13, 0
	v_fmac_f32_e32 v188, v82, v208
	s_cmp_eq_u32 s12, 0xb4000
	v_lshl_add_u64 v[116:117], v[116:117], 0, s[44:45]
	s_cbranch_scc1 .LBB0_718
	s_mov_b32 s6, s89
	s_mov_b32 s89, s61
	v_mov_b32_e32 v207, v202
	s_branch .LBB0_666

; DEVI f32x4 ld_nt(const float* p) { return __builtin_nontemporal_load((const f32x4*)p); }
; DEVI CvSlice cv_slice(const Params& p, int l, int s, int lane) {
;     CvSlice c;
;     if (s < NS_W13) {
;         const int e = s >> 9, r = s & 511, hb = r & 7, mat = (r >> 3) & 1, ks = r >> 4;
;         const float* W = mat ? (e < NE ? p.w3 + ((size_t)l * NE + e) * 1024 * 256 : p.ws3 + (size_t)l * 1024 * 256)
;                              : (e < NE ? p.w1 + ((size_t)l * NE + e) * 1024 * 256 : p.ws1 + (size_t)l * 1024 * 256);
;         const int hc0 = hb * 32;
;         c.src = W + hc0 + (lane & 7) * 4; c.ld = 256; c.dst = p.w13t + (size_t)e * 512 * 1024; c.K = 1024;
;         c.r0 = (hc0 >> 7) * 256 + ((hc0 >> 5) & 3) * 32 + mat * 16; c.k0 = ks * 32; c.perm = 0;
;     } else {
;         s -= NS_W13;
;         const int e = s >> 8, r = s & 255, nb = r & 31, ks = r >> 5;
;         const float* W2 = e < NE ? p.w2 + ((size_t)l * NE + e) * 256 * 1024 : p.ws2 + (size_t)l * 256 * 1024;
;         c.src = W2 + nb * 32 + (lane & 7) * 4; c.ld = 1024; c.dst = p.w2t + (size_t)e * 1024 * 256; c.K = 256; c.r0 = (nb >> 3) * 256 + ((nb & 7) >> 1) * 32 + (nb & 1) * 8; c.k0 = ks * 32; c.perm = 1;
;     }
;     return c;
; }
; DEVI void cv_next(const Params& p, int l, int s, int lane, int stride, CvRun& run) {
;     ...
;     run.c = cv_slice(p, l, s, lane); run.left = 0;
;     if ((stride & 511) == 0) {
;         if (s < NS_W13) { const int e = s >> 9, es = stride >> 9; if (e < NE) { run.left = (NE - 1 - e) / es; run.sstep = (long)es * 1024 * 256; run.dstep = (long)es * 512 * 1024; } }
;         else { const int e = (s - NS_W13) >> 8, es = stride >> 8; if (e < NE) { run.left = (NE - 1 - e) / es; run.sstep = (long)es * 256 * 1024; run.dstep = (long)es * 1024 * 256; } } }
; }
; DEVI void cv_issue(const Params& p, int l, int s, int lane, CvRegs& R, CvRun& run) {
;     R.live = s < NS_SLICES ? 1 : 0;
;     if (R.live) { cv_next(p, l, s, lane, (int)gridDim.x * 8, run); R.c = run.c; const int kq = lane >> 3;
;         const float* sp = R.c.src + (size_t)(R.c.k0 + 2 * kq) * R.c.ld;
;         R.a0 = ld_nt(sp); R.b0 = ld_nt(sp + R.c.ld); R.a1 = ld_nt(sp + (size_t)16 * R.c.ld); R.b1 = ld_nt(sp + (size_t)17 * R.c.ld); }
.LBB0_2230:
	s_mul_i32 s98, s71, 0x6000
	s_add_i32 s98, s98, 0
	v_add_u32_e32 v86, s98, v129
	ds_read_b128 v[82:85], v86 offset:12288
	ds_read_b128 v[124:127], v86 offset:18432
	s_cmp_lt_i32 s54, 0x30300
	s_mov_b32 s2, s61
	s_cselect_b64 s[14:15], -1, 0
	s_cmp_gt_i32 s54, 0x302ff
	s_mov_b32 s61, s6
	s_cbranch_scc1 .LBB0_2260
	s_cmp_lt_i32 s56, 1
	s_mov_b64 s[16:17], -1
	s_cbranch_scc0 .LBB0_2257
	s_lshl_b32 s84, s54, 5
	s_lshl_b32 s85, s54, 4
	s_lshl_b32 s88, s54, 3
	s_lshl_b32 s70, s54, 1
	s_lshl_b32 s89, s54, 10
	s_add_i32 s89, s89, 0xf7f80000
	s_cmp_gt_i32 s54, 0x201ff
	s_cselect_b64 s[16:17], -1, 0
	s_mov_b64 s[6:7], -1
	s_and_b64 vcc, exec, s[16:17]
	s_cbranch_vccz .LBB0_2234
	s_add_i32 s6, s54, 0xfffdfe00
	s_lshr_b32 s8, s6, 8
	s_and_b32 s10, s54, 0xe0
	s_cmp_lt_u32 s6, 0x10000
	s_cselect_b64 s[6:7], -1, 0
	s_and_b32 s11, s89, 0x3fc0000
	s_bitset1_b32 s11, 26
	s_and_b64 s[6:7], s[6:7], exec
	s_cselect_b32 s6, 0xc0, s79
	s_cselect_b32 s11, s11, 0x40000
	s_add_u32 s6, s24, s6
	s_addc_u32 s7, s25, 0
	s_load_dwordx2 s[6:7], s[6:7], 0x0
	s_lshl_b32 s11, s11, 2
	s_load_dwordx2 s[20:21], s[24:25], 0x158
	s_waitcnt lgkmcnt(0)
	s_add_u32 s6, s6, s11
	s_addc_u32 s7, s7, 0
	s_and_b32 s11, s84, 0x3e0
	s_lshl_b32 s11, s11, 2
	s_add_u32 s18, s6, s11
	s_addc_u32 s19, s7, 0
	s_lshl_b64 s[6:7], s[8:9], 19
	s_add_u32 s20, s20, s6
	s_addc_u32 s21, s21, s7
	s_and_b32 s6, s84, 0x300
	s_and_b32 s7, s85, 0x60
	s_or_b32 s6, s6, s7
	s_and_b32 s7, s88, 8
	s_or_b32 s8, s6, s7
	s_mov_b64 s[6:7], 0

; template <bool FIRST> DEVI bool partialSM(f32x16& p0, f32x16& p1, float& m_reg, float& alpha) {
;     float pmax = p0[0];
; #pragma unroll
;     for (int r = 1; r < 16; ++r) pmax = fmaxf(pmax, p0[r]);
; #pragma unroll
;     for (int r = 0; r < 16; ++r) pmax = fmaxf(pmax, p1[r]);
;     { auto rr = __builtin_amdgcn_permlane32_swap(__float_as_uint(pmax), __float_as_uint(pmax), false, false);
;       pmax = fmaxf(__uint_as_float(rr[0]), __uint_as_float(rr[1])); }
;     if (FIRST) { m_reg = pmax; alpha = 1.f;
; #pragma unroll
;         for (int r = 0; r < 16; ++r) { p0[r] = __builtin_amdgcn_exp2f(p0[r] - pmax); p1[r] = p1[r] - pmax; }
;         return false;
;     } else if (__builtin_expect(__all(pmax <= ATT_THR), 1)) { alpha = 1.f;
; #pragma unroll
;         for (int r = 0; r < 16; ++r) p0[r] = __builtin_amdgcn_exp2f(p0[r]);
;         return false;
;     } else { const float d = fmaxf(pmax, 0.f); alpha = __builtin_amdgcn_exp2f(-d); m_reg += d;
; #pragma unroll
;         for (int r = 0; r < 16; ++r) { p0[r] = __builtin_amdgcn_exp2f(p0[r] - d); p1[r] = p1[r] - d; }
;         return true;
;     }
; }
; DEVI void finishSM(f32x16& p0, f32x16& p1, float alpha, float& l_reg, bf16x8& pa0, bf16x8& pa1, bf16x8& pa2, bf16x8& pa3) {
; #pragma unroll
;     for (int r = 0; r < 16; ++r) p1[r] = __builtin_amdgcn_exp2f(p1[r]);
;     f32x2 s2 = (f32x2){p0[0], p0[1]} + (f32x2){p1[0], p1[1]};
; #pragma unroll
;     for (int r = 2; r < 16; r += 2) s2 += (f32x2){p0[r], p0[r + 1]} + (f32x2){p1[r], p1[r + 1]};
;     float ps = s2[0] + s2[1];
;     { auto rr = __builtin_amdgcn_permlane32_swap(__float_as_uint(ps), __float_as_uint(ps), false, false);
;       ps = __uint_as_float(rr[0]) + __uint_as_float(rr[1]); }
;     l_reg = l_reg * alpha + ps;
;     ...
;     PK4(p0, 0, pa0); PK4(p0, 8, pa1); PK4(p1, 0, pa2); PK4(p1, 8, pa3);
;     ...
; }
; DEVI void qkt(f32x16& p0, f32x16& p1, const char* Kb, const bf16x8 (&qr)[6], int r32, int hi, const f32x16& cinit) {
; #pragma unroll
;     for (int d0 = 0; d0 < 6; ++d0) { const int cb = (d0 * 16 + hi * 8) * 2;
;         const bf16x8 k0 = *(const bf16x8*)(Kb + KSWZ(r32, cb)), k1 = *(const bf16x8*)(Kb + KSWZ(32 + r32, cb));
;         p0 = __builtin_amdgcn_mfma_f32_32x32x16_bf16(k0, qr[d0], d0 == 0 ? cinit : p0, 0, 0, 0);
;         p1 = __builtin_amdgcn_mfma_f32_32x32x16_bf16(k1, qr[d0], d0 == 0 ? cinit : p1, 0, 0, 0); }
; }
.LBB0_2260:
	v_add_u32_e32 v174, s98, v205
	v_exp_f32_e32 v66, v66
	v_exp_f32_e32 v67, v67
	s_waitcnt lgkmcnt(0)
	v_mfma_f32_32x32x16_bf16 v[98:113], v[82:85], v[150:153], v[34:49]
	v_add_u32_e32 v82, s98, v184
	v_add_u32_e32 v83, s98, v185
	ds_read_b128 v[210:213], v82 offset:12288
	ds_read_b128 v[214:217], v82 offset:18432
	ds_read_b128 v[218:221], v83 offset:12288
	ds_read_b128 v[222:225], v83 offset:18432
	v_exp_f32_e32 v68, v68
	v_exp_f32_e32 v69, v69
	v_exp_f32_e32 v70, v70
	v_exp_f32_e32 v71, v71
	s_waitcnt lgkmcnt(4)
	v_mfma_f32_32x32x16_bf16 v[82:97], v[124:127], v[150:153], v[34:49]
	ds_read_b128 v[124:127], v174 offset:12288
	ds_read_b128 v[226:229], v174 offset:18432
	v_exp_f32_e32 v72, v72
	v_exp_f32_e32 v73, v73
	v_exp_f32_e32 v74, v74
	v_exp_f32_e32 v75, v75
	v_exp_f32_e32 v76, v76
	v_exp_f32_e32 v77, v77
	s_waitcnt lgkmcnt(0)
	v_mfma_f32_32x32x16_bf16 v[98:113], v[210:213], v[138:141], v[98:113]
	v_add_u32_e32 v174, s98, v206
	v_exp_f32_e32 v78, v78
	v_exp_f32_e32 v79, v79
	ds_read_b128 v[230:233], v174 offset:12288
	ds_read_b128 v[234:237], v174 offset:18432
	v_exp_f32_e32 v80, v80
	v_exp_f32_e32 v81, v81
	v_add_u32_e32 v174, s98, v207
	s_waitcnt lgkmcnt(6)
	v_mfma_f32_32x32x16_bf16 v[82:97], v[214:217], v[138:141], v[82:97]
	v_pk_add_f32 v[214:215], v[50:51], v[66:67]
	v_pk_add_f32 v[216:217], v[52:53], v[68:69]
	v_lshl_add_u32 v203, s71, 14, v115
	v_pk_add_f32 v[214:215], v[216:217], v[214:215]
	v_pk_add_f32 v[216:217], v[54:55], v[70:71]
	ds_read_b128 v[210:213], v174 offset:12288
	ds_read_b128 v[238:241], v174 offset:18432
	v_pk_add_f32 v[214:215], v[216:217], v[214:215]
	s_waitcnt lgkmcnt(7)
	v_mfma_f32_32x32x16_bf16 v[98:113], v[218:221], v[134:137], v[98:113]
	v_pk_add_f32 v[216:217], v[56:57], v[72:73]
	v_cvt_pk_bf16_f32 v50, v50, v51
	v_cvt_pk_bf16_f32 v51, v52, v53
	v_cvt_pk_bf16_f32 v52, v54, v55
	v_cvt_pk_bf16_f32 v53, v56, v57
	v_cvt_pk_bf16_f32 v54, v58, v59
	v_pk_add_f32 v[214:215], v[216:217], v[214:215]
	s_waitcnt lgkmcnt(6)
	v_mfma_f32_32x32x16_bf16 v[82:97], v[222:225], v[134:137], v[82:97]
	v_pk_add_f32 v[216:217], v[58:59], v[74:75]
	v_cvt_pk_bf16_f32 v55, v60, v61
	v_cvt_pk_bf16_f32 v56, v62, v63
	v_cvt_pk_bf16_f32 v57, v64, v65
	v_cvt_pk_bf16_f32 v58, v66, v67
	v_cvt_pk_bf16_f32 v59, v68, v69
	v_pk_add_f32 v[214:215], v[216:217], v[214:215]
	s_waitcnt lgkmcnt(5)
	v_mfma_f32_32x32x16_bf16 v[98:113], v[124:127], v[130:133], v[98:113]
	v_pk_add_f32 v[216:217], v[60:61], v[76:77]
	v_pk_add_f32 v[126:127], v[62:63], v[78:79]
	v_pk_add_f32 v[124:125], v[216:217], v[214:215]
	v_cvt_pk_bf16_f32 v60, v70, v71
	v_cvt_pk_bf16_f32 v61, v72, v73
	v_cvt_pk_bf16_f32 v62, v74, v75
	v_cvt_pk_bf16_f32 v63, v76, v77
	s_waitcnt lgkmcnt(4)
	v_mfma_f32_32x32x16_bf16 v[82:97], v[226:229], v[130:133], v[82:97]
	v_pk_add_f32 v[124:125], v[126:127], v[124:125]
	v_pk_add_f32 v[126:127], v[64:65], v[80:81]
	v_cvt_pk_bf16_f32 v64, v78, v79
	v_cvt_pk_bf16_f32 v65, v80, v81
	ds_read_b64_tr_b16 v[66:67], v203 offset:0
	ds_read_b64_tr_b16 v[68:69], v203 offset:0x400
	ds_read_b64_tr_b16 v[70:71], v203 offset:0x800
	s_waitcnt lgkmcnt(0)
	v_mfma_f32_32x32x16_bf16 v[98:113], v[230:233], v[146:149], v[98:113]
	ds_read_b64_tr_b16 v[72:73], v203 offset:0xc00
	ds_read_b64_tr_b16 v[74:75], v203 offset:0x1000
	ds_read_b64_tr_b16 v[76:77], v203 offset:0x1400
	ds_read_b64_tr_b16 v[78:79], v203 offset:0x1800
	ds_read_b64_tr_b16 v[80:81], v203 offset:0x1c00
	v_pk_add_f32 v[124:125], v[126:127], v[124:125]
	s_waitcnt lgkmcnt(2)
	v_mfma_f32_32x32x16_bf16 v[82:97], v[234:237], v[146:149], v[82:97]
	v_pk_add_f32 v[124:125], v[124:125], v[124:125] op_sel:[0,1] op_sel_hi:[1,0]
	s_nop 0
	v_mov_b32_e32 v125, v124
	s_nop 1
	v_permlane32_swap_b32_e32 v124, v125
	s_waitcnt lgkmcnt(1)
	v_mfma_f32_32x32x16_bf16 v[98:113], v[210:213], v[142:145], v[98:113]
	ds_read_b64_tr_b16 v[210:211], v203 offset:0x200
	ds_read_b64_tr_b16 v[212:213], v203 offset:0x600
	ds_read_b64_tr_b16 v[214:215], v203 offset:0xa00
	ds_read_b64_tr_b16 v[216:217], v203 offset:0xe00
	ds_read_b64_tr_b16 v[218:219], v203 offset:0x1200
	ds_read_b64_tr_b16 v[220:221], v203 offset:0x1600
	ds_read_b64_tr_b16 v[222:223], v203 offset:0x1a00
	s_waitcnt lgkmcnt(0)
	v_mfma_f32_32x32x16_bf16 v[82:97], v[238:241], v[142:145], v[82:97]
	ds_read_b64_tr_b16 v[224:225], v203 offset:0x1e00
	s_waitcnt lgkmcnt(8)
	v_mfma_f32_32x32x16_bf16 v[18:33], v[50:53], v[66:69], v[18:33]
	s_waitcnt lgkmcnt(0)
	v_mfma_f32_32x32x16_bf16 v[18:33], v[54:57], v[70:73], v[18:33]
	v_mfma_f32_32x32x16_bf16 v[18:33], v[58:61], v[74:77], v[18:33]
	v_mfma_f32_32x32x16_bf16 v[18:33], v[62:65], v[78:81], v[18:33]
	v_mfma_f32_32x32x16_bf16 v[2:17], v[50:53], v[210:213], v[2:17]
	s_nop 4
	v_max_f32_e32 v249, v99, v99
	v_max_f32_e32 v250, v98, v98
	v_max_f32_e32 v249, v250, v249
	v_max3_f32 v249, v249, v100, v101
	v_max3_f32 v249, v249, v102, v103
	v_max3_f32 v251, v249, v104, v105
	v_max3_f32 v251, v251, v106, v107
	v_exp_f32_e32 v50, v98
	v_exp_f32_e32 v51, v99
	v_exp_f32_e32 v52, v100
	v_exp_f32_e32 v53, v101
	v_mov_b64_e32 v[66:67], v[82:83]
	v_mov_b64_e32 v[68:69], v[84:85]
	v_mfma_f32_32x32x16_bf16 v[2:17], v[54:57], v[214:217], v[2:17]
	v_max3_f32 v251, v251, v108, v109
	v_max3_f32 v251, v251, v110, v111
	v_max3_f32 v251, v251, v112, v113
	v_max3_f32 v251, v251, v82, v83
	v_max3_f32 v251, v251, v84, v85
	v_max3_f32 v251, v251, v86, v87
	v_max3_f32 v251, v251, v88, v89
	v_exp_f32_e32 v54, v102
	v_exp_f32_e32 v55, v103
	v_exp_f32_e32 v56, v104
	v_exp_f32_e32 v57, v105
	v_mov_b64_e32 v[70:71], v[86:87]
	v_mov_b64_e32 v[72:73], v[88:89]
	v_mfma_f32_32x32x16_bf16 v[2:17], v[58:61], v[218:221], v[2:17]
	v_max3_f32 v251, v251, v90, v91
	v_max3_f32 v251, v251, v92, v93
	v_max3_f32 v251, v251, v94, v95
	v_max3_f32 v251, v251, v96, v97
	v_mov_b32_e32 v252, v251
	s_nop 1
	v_permlane32_swap_b32_e32 v251, v252
	v_exp_f32_e32 v58, v106
	v_exp_f32_e32 v59, v107
	v_exp_f32_e32 v60, v108
	v_exp_f32_e32 v61, v109
	v_mov_b64_e32 v[74:75], v[90:91]
	v_mov_b64_e32 v[76:77], v[92:93]
	v_mfma_f32_32x32x16_bf16 v[2:17], v[62:65], v[222:225], v[2:17]
	v_exp_f32_e32 v62, v110
	v_exp_f32_e32 v63, v111
	v_exp_f32_e32 v64, v112
	v_exp_f32_e32 v65, v113
	v_mov_b64_e32 v[78:79], v[94:95]
	v_mov_b64_e32 v[80:81], v[96:97]
	v_max_f32_e32 v252, v252, v252
	v_max_f32_e32 v251, v251, v251
	v_max_f32_e32 v126, v251, v252
	v_cmp_ge_f32_e32 vcc, s80, v126
	s_cmp_lg_u64 vcc, exec
	s_cselect_b64 s[6:7], -1, 0
	s_cbranch_scc1 .LBB0_2269
	v_mov_b32_e32 v209, 1.0
	v_mov_b32_e32 v210, v204
	s_branch .LBB0_2263

; template <bool FIRST> DEVI bool partialSM(f32x16& p0, f32x16& p1, float& m_reg, float& alpha) {
;     float pmax = p0[0];
; #pragma unroll
;     for (int r = 1; r < 16; ++r) pmax = fmaxf(pmax, p0[r]);
; #pragma unroll
;     for (int r = 0; r < 16; ++r) pmax = fmaxf(pmax, p1[r]);
;     { auto rr = __builtin_amdgcn_permlane32_swap(__float_as_uint(pmax), __float_as_uint(pmax), false, false);
;       pmax = fmaxf(__uint_as_float(rr[0]), __uint_as_float(rr[1])); }
;     if (FIRST) { m_reg = pmax; alpha = 1.f;
; #pragma unroll
;         for (int r = 0; r < 16; ++r) { p0[r] = __builtin_amdgcn_exp2f(p0[r] - pmax); p1[r] = p1[r] - pmax; }
;         return false;
;     } else if (__builtin_expect(__all(pmax <= ATT_THR), 1)) { alpha = 1.f;
; #pragma unroll
;         for (int r = 0; r < 16; ++r) p0[r] = __builtin_amdgcn_exp2f(p0[r]);
;         return false;
;     } else { const float d = fmaxf(pmax, 0.f); alpha = __builtin_amdgcn_exp2f(-d); m_reg += d;
; #pragma unroll
;         for (int r = 0; r < 16; ++r) { p0[r] = __builtin_amdgcn_exp2f(p0[r] - d); p1[r] = p1[r] - d; }
;         return true;
;     }
; }
; DEVI void finishSM(f32x16& p0, f32x16& p1, float alpha, float& l_reg, bf16x8& pa0, bf16x8& pa1, bf16x8& pa2, bf16x8& pa3) {
; #pragma unroll
;     for (int r = 0; r < 16; ++r) p1[r] = __builtin_amdgcn_exp2f(p1[r]);
;     f32x2 s2 = (f32x2){p0[0], p0[1]} + (f32x2){p1[0], p1[1]};
; #pragma unroll
;     for (int r = 2; r < 16; r += 2) s2 += (f32x2){p0[r], p0[r + 1]} + (f32x2){p1[r], p1[r + 1]};
;     float ps = s2[0] + s2[1];
;     { auto rr = __builtin_amdgcn_permlane32_swap(__float_as_uint(ps), __float_as_uint(ps), false, false);
;       ps = __uint_as_float(rr[0]) + __uint_as_float(rr[1]); }
;     l_reg = l_reg * alpha + ps;
;     ...
;     PK4(p0, 0, pa0); PK4(p0, 8, pa1); PK4(p1, 0, pa2); PK4(p1, 8, pa3);
;     ...
; }
; DEVI void qkt(f32x16& p0, f32x16& p1, const char* Kb, const bf16x8 (&qr)[6], int r32, int hi, const f32x16& cinit) {
; #pragma unroll
;     for (int d0 = 0; d0 < 6; ++d0) { const int cb = (d0 * 16 + hi * 8) * 2;
;         const bf16x8 k0 = *(const bf16x8*)(Kb + KSWZ(r32, cb)), k1 = *(const bf16x8*)(Kb + KSWZ(32 + r32, cb));
;         p0 = __builtin_amdgcn_mfma_f32_32x32x16_bf16(k0, qr[d0], d0 == 0 ? cinit : p0, 0, 0, 0);
;         p1 = __builtin_amdgcn_mfma_f32_32x32x16_bf16(k1, qr[d0], d0 == 0 ? cinit : p1, 0, 0, 0); }
; }
.LBB0_2266:
	s_mul_i32 s98, s61, 0x6000
	s_add_i32 s98, s96, s98
	s_lshl_b32 s99, s61, 14
	s_add_i32 s99, s97, s99
	s_mul_i32 s6, s2, 0x6000
	s_add_i32 s6, s6, 0
	v_add_u32_e32 v86, s6, v129
	v_lshl_add_u64 v[250:251], v[118:119], 0, s[12:13]
	s_mov_b32 m0, s98
	s_barrier
	ds_read_b128 v[82:85], v86
	ds_read_b128 v[212:215], v86 offset:6144
	global_load_lds_dwordx4 v[250:251], off
	v_exp_f32_e32 v66, v66
	s_waitcnt lgkmcnt(0)
	v_mfma_f32_32x32x16_bf16 v[98:113], v[82:85], v[150:153], v[34:49]
	v_add_u32_e32 v126, s6, v184
	v_lshl_add_u64 v[250:251], v[120:121], 0, s[12:13]
	s_add_i32 m0, s98, 0x2000
	v_exp_f32_e32 v67, v67
	v_exp_f32_e32 v68, v68
	global_load_lds_dwordx4 v[250:251], off
	v_exp_f32_e32 v69, v69
	v_exp_f32_e32 v70, v70
	v_exp_f32_e32 v71, v71
	v_exp_f32_e32 v72, v72
	v_mfma_f32_32x32x16_bf16 v[82:97], v[212:215], v[150:153], v[34:49]
	ds_read_b128 v[212:215], v126
	ds_read_b128 v[216:219], v126 offset:6144
	v_add_u32_e32 v126, s6, v185
	v_lshl_add_u64 v[250:251], v[122:123], 0, s[12:13]
	s_add_i32 m0, s98, 0x4000
	v_exp_f32_e32 v73, v73
	v_exp_f32_e32 v74, v74
	global_load_lds_dwordx4 v[250:251], off
	v_exp_f32_e32 v75, v75
	v_exp_f32_e32 v76, v76
	v_exp_f32_e32 v77, v77
	s_waitcnt lgkmcnt(0)
	v_mfma_f32_32x32x16_bf16 v[98:113], v[212:215], v[138:141], v[98:113]
	s_mov_b32 m0, s99
	v_exp_f32_e32 v78, v78
	v_exp_f32_e32 v79, v79
	v_lshl_add_u64 v[250:251], v[116:117], 0, s[40:41]
	global_load_lds_dwordx4 v[116:117], off
	s_add_i32 m0, s99, 0x2000
	v_exp_f32_e32 v80, v80
	v_exp_f32_e32 v81, v81
	v_add_u32_e32 v174, 0x2000, v203
	global_load_lds_dwordx4 v[250:251], off
	v_mfma_f32_32x32x16_bf16 v[82:97], v[216:219], v[138:141], v[82:97]
	ds_read_b128 v[212:215], v126
	ds_read_b128 v[216:219], v126 offset:6144
	v_add_u32_e32 v126, s6, v205
	s_waitcnt lgkmcnt(0)
	v_mfma_f32_32x32x16_bf16 v[98:113], v[212:215], v[134:137], v[98:113]
	ds_read_b128 v[212:215], v126
	ds_read_b128 v[220:223], v126 offset:6144
	v_add_u32_e32 v126, s6, v206
	v_mfma_f32_32x32x16_bf16 v[82:97], v[216:219], v[134:137], v[82:97]
	ds_read_b128 v[216:219], v126
	ds_read_b128 v[224:227], v126 offset:6144
	v_add_u32_e32 v126, s6, v207
	ds_read_b128 v[228:231], v126
	ds_read_b128 v[232:235], v126 offset:6144
	v_pk_add_f32 v[126:127], v[50:51], v[66:67]
	v_cvt_pk_bf16_f32 v50, v50, v51
	v_cvt_pk_bf16_f32 v51, v52, v53
	s_waitcnt lgkmcnt(0)
	v_mfma_f32_32x32x16_bf16 v[98:113], v[212:215], v[130:133], v[98:113]
	v_pk_add_f32 v[212:213], v[52:53], v[68:69]
	v_cvt_pk_bf16_f32 v52, v54, v55
	v_cvt_pk_bf16_f32 v53, v56, v57
	v_pk_add_f32 v[126:127], v[212:213], v[126:127]
	v_pk_add_f32 v[212:213], v[54:55], v[70:71]
	v_cvt_pk_bf16_f32 v54, v58, v59
	v_mfma_f32_32x32x16_bf16 v[82:97], v[220:223], v[130:133], v[82:97]
	v_pk_add_f32 v[126:127], v[212:213], v[126:127]
	v_pk_add_f32 v[212:213], v[56:57], v[72:73]
	v_cvt_pk_bf16_f32 v55, v60, v61
	v_cvt_pk_bf16_f32 v56, v62, v63
	v_cvt_pk_bf16_f32 v57, v64, v65
	v_pk_add_f32 v[126:127], v[212:213], v[126:127]
	v_pk_add_f32 v[212:213], v[58:59], v[74:75]
	v_cvt_pk_bf16_f32 v58, v66, v67
	v_cvt_pk_bf16_f32 v59, v68, v69
	v_mfma_f32_32x32x16_bf16 v[98:113], v[216:219], v[146:149], v[98:113]
	v_pk_add_f32 v[126:127], v[212:213], v[126:127]
	v_pk_add_f32 v[212:213], v[60:61], v[76:77]
	v_cvt_pk_bf16_f32 v60, v70, v71
	v_cvt_pk_bf16_f32 v61, v72, v73
	v_pk_add_f32 v[126:127], v[212:213], v[126:127]
	v_pk_add_f32 v[212:213], v[62:63], v[78:79]
	v_cvt_pk_bf16_f32 v62, v74, v75
	v_cvt_pk_bf16_f32 v63, v76, v77
	v_mfma_f32_32x32x16_bf16 v[82:97], v[224:227], v[146:149], v[82:97]
	v_pk_add_f32 v[126:127], v[212:213], v[126:127]
	v_pk_add_f32 v[212:213], v[64:65], v[80:81]
	v_cvt_pk_bf16_f32 v64, v78, v79
	v_cvt_pk_bf16_f32 v65, v80, v81
	ds_read_b64_tr_b16 v[66:67], v174 offset:0
	ds_read_b64_tr_b16 v[68:69], v174 offset:0x400
	ds_read_b64_tr_b16 v[70:71], v174 offset:0x800
	ds_read_b64_tr_b16 v[72:73], v174 offset:0xc00
	ds_read_b64_tr_b16 v[74:75], v174 offset:0x1000
	ds_read_b64_tr_b16 v[76:77], v174 offset:0x1400
	ds_read_b64_tr_b16 v[78:79], v174 offset:0x1800
	ds_read_b64_tr_b16 v[80:81], v174 offset:0x1c00
	v_pk_add_f32 v[126:127], v[212:213], v[126:127]
	ds_read_b64_tr_b16 v[212:213], v174 offset:0x200
	ds_read_b64_tr_b16 v[214:215], v174 offset:0x600
	ds_read_b64_tr_b16 v[216:217], v174 offset:0xa00
	v_mfma_f32_32x32x16_bf16 v[98:113], v[228:231], v[142:145], v[98:113]
	ds_read_b64_tr_b16 v[218:219], v174 offset:0xe00
	ds_read_b64_tr_b16 v[220:221], v174 offset:0x1200
	ds_read_b64_tr_b16 v[222:223], v174 offset:0x1600
	ds_read_b64_tr_b16 v[224:225], v174 offset:0x1a00
	ds_read_b64_tr_b16 v[226:227], v174 offset:0x1e00
	v_pk_add_f32 v[126:127], v[126:127], v[126:127] op_sel:[0,1] op_sel_hi:[1,0]
	s_waitcnt lgkmcnt(8)
	v_mfma_f32_32x32x16_bf16 v[82:97], v[232:235], v[142:145], v[82:97]
	v_mov_b32_e32 v127, v126
	s_nop 1
	v_permlane32_swap_b32_e32 v126, v127
	v_mfma_f32_32x32x16_bf16 v[18:33], v[50:53], v[66:69], v[18:33]
	s_waitcnt lgkmcnt(0)
	v_mfma_f32_32x32x16_bf16 v[18:33], v[54:57], v[70:73], v[18:33]
	v_mfma_f32_32x32x16_bf16 v[18:33], v[58:61], v[74:77], v[18:33]
	v_mfma_f32_32x32x16_bf16 v[18:33], v[62:65], v[78:81], v[18:33]
	v_mfma_f32_32x32x16_bf16 v[2:17], v[50:53], v[212:215], v[2:17]
	s_nop 0
	v_max_f32_e32 v249, v99, v99
	v_max_f32_e32 v250, v98, v98
	v_max_f32_e32 v249, v250, v249
	v_max3_f32 v249, v249, v100, v101
	v_max3_f32 v249, v249, v102, v103
	v_max3_f32 v251, v249, v104, v105
	v_max3_f32 v251, v251, v106, v107
	v_exp_f32_e32 v50, v98
	v_exp_f32_e32 v51, v99
	v_exp_f32_e32 v52, v100
	v_exp_f32_e32 v53, v101
	v_mov_b64_e32 v[66:67], v[82:83]
	v_mov_b64_e32 v[68:69], v[84:85]
	v_mfma_f32_32x32x16_bf16 v[2:17], v[54:57], v[216:219], v[2:17]
	v_max3_f32 v251, v251, v108, v109
	v_max3_f32 v251, v251, v110, v111
	v_max3_f32 v251, v251, v112, v113
	v_max3_f32 v251, v251, v82, v83
	v_max3_f32 v251, v251, v84, v85
	v_max3_f32 v251, v251, v86, v87
	v_max3_f32 v251, v251, v88, v89
	v_exp_f32_e32 v54, v102
	v_exp_f32_e32 v55, v103
	v_exp_f32_e32 v56, v104
	v_exp_f32_e32 v57, v105
	v_mov_b64_e32 v[70:71], v[86:87]
	v_mov_b64_e32 v[72:73], v[88:89]
	v_mfma_f32_32x32x16_bf16 v[2:17], v[58:61], v[220:223], v[2:17]
	v_max3_f32 v251, v251, v90, v91
	v_max3_f32 v251, v251, v92, v93
	v_max3_f32 v251, v251, v94, v95
	v_max3_f32 v251, v251, v96, v97
	v_mov_b32_e32 v252, v251
	s_nop 1
	v_permlane32_swap_b32_e32 v251, v252
	v_exp_f32_e32 v58, v106
	v_exp_f32_e32 v59, v107
	v_exp_f32_e32 v60, v108
	v_exp_f32_e32 v61, v109
	v_mov_b64_e32 v[74:75], v[90:91]
	v_mov_b64_e32 v[76:77], v[92:93]
	v_mfma_f32_32x32x16_bf16 v[2:17], v[62:65], v[224:227], v[2:17]
	v_exp_f32_e32 v62, v110
	v_exp_f32_e32 v63, v111
	v_exp_f32_e32 v64, v112
	v_exp_f32_e32 v65, v113
	v_mov_b64_e32 v[78:79], v[94:95]
	v_mov_b64_e32 v[80:81], v[96:97]
	v_max_f32_e32 v252, v252, v252
	v_max_f32_e32 v251, v251, v251
	v_max_f32_e32 v174, v251, v252
	v_cmp_ge_f32_e32 vcc, s80, v174
	s_cmp_lg_u64 vcc, exec
	s_cselect_b64 s[6:7], -1, 0
	s_cbranch_scc1 .LBB0_2275
	v_mov_b32_e32 v203, 1.0
	v_mov_b32_e32 v204, v210
	s_branch .LBB0_2280

; #define VM0() asm volatile("s_waitcnt vmcnt(0)" ::: "memory")
; #define B_RESC(a, rare) do { if (rare) { if (hi == 0) al_l[r32] = (a); asm volatile("s_waitcnt lgkmcnt(0)" ::: "memory"); __builtin_amdgcn_wave_barrier(); \
;         _Pragma("unroll") for (int _d = 0; _d < 2; ++_d) _Pragma("unroll") for (int _r = 0; _r < 16; ++_r) o[_d][_r] *= al_l[crow(_r, hi)]; C_SPLAT(); } } while (0)
; DEVI void attn_unit8(const Params& p, char* smem, int unit, int l, int& cvs  , CvRun& crun) {
;     ...
;     for (int T = 0; T + 1 < NTILE; ++T) {
;         const char* Kb = K_lds + s0 * 24576; const int vb = vb0 + s0 * 16384;
;         CvRegs cvr; cv_issue(p, l, cvs, lane, cvr, crun); cvs += (int)gridDim.x * 8;
;         qkt(pB0, pB1, Kb + 12288, qr, r32, hi, cinit);
;         finishSM(pA0, pA1, alA, l_reg, pa0, pa1, pa2, pa3);
;         pv_both(o[0], o[1], vb, pa0, pa1, pa2, pa3);
;         { const bool rr_ = partialSM<false>(pB0, pB1, m_reg, alB); B_RESC(alB, rr_); }
;         cv_finish(smem + 124928 + wid * 2304, lane, cvr);
;         if (cvr.live) asm volatile("s_waitcnt vmcnt(2)" ::: "memory"); else VM0();
;         __syncthreads();
;         if (T + 2 < NTILE) B_DMA(T + 2, s2);
;         qkt(pA0, pA1, K_lds + s1 * 24576, qr, r32, hi, cinit);
;         finishSM(pB0, pB1, alB, l_reg, pa0, pa1, pa2, pa3);
;         pv_both(o[0], o[1], vb + 8192, pa0, pa1, pa2, pa3);
;         { const bool rr_ = partialSM<false>(pA0, pA1, m_reg, alA); B_RESC(alA, rr_); }
;         { const int t = s0; s0 = s1; s1 = s2; s2 = t; }
;     }
.LBB0_2280:
	s_add_i32 s54, s54, s86
	v_add_f32_e32 v82, v124, v125
	s_add_u32 s12, s12, 0x6000
	v_fmac_f32_e32 v82, v189, v208
	v_add_f32_e32 v189, v126, v127
	s_addc_u32 s13, s13, 0
	v_fmac_f32_e32 v189, v82, v209
	s_cmp_eq_u32 s12, 0xb4000
	v_lshl_add_u64 v[116:117], v[116:117], 0, s[44:45]
	s_cbranch_scc1 .LBB0_2282
	s_mov_b32 s6, s71
	s_mov_b32 s71, s2
	v_mov_b32_e32 v208, v203
	s_branch .LBB0_2230
